# baseline (speedup 1.0000x reference)
_Z11attn_kernelPKDF16_S0_S0_S0_PDF16_:
	s_load_dwordx8 s[68:75], s[0:1], 0x0
	s_load_dwordx2 s[36:37], s[0:1], 0x20
	s_lshl_b32 s0, s2, 2
	s_and_b32 s0, s0, 28
	s_lshr_b32 s3, s2, 6
	v_readfirstlane_b32 s1, v0
	s_add_i32 s38, s0, s3
	s_mov_b32 s39, 0
	s_lshr_b32 s33, s1, 8
	s_cmp_eq_u32 s33, 0
	s_cbranch_scc0 .Lmy_noprio
	s_setprio 1
